# speedup vs baseline: 1.0257x; 1.0190x over previous
_Z8k3_chainPKfPK15HIP_vector_typeIiLj4EEPKtS6_S0_S0_Pf:
	s_load_dwordx8 s[8:15], s[0:1], 0x0
	s_load_dwordx4 s[4:7], s[0:1], 0x20
	s_load_dwordx2 s[16:17], s[0:1], 0x30
	s_mul_hi_u32 s0, s2, 0xaaaaaaab
	s_lshr_b32 s20, s0, 5
	s_mul_i32 s0, s20, 48
	s_mov_b32 s21, 0
	s_sub_i32 s18, s2, s0
	s_lshl_b64 s[0:1], s[20:21], 13
	s_waitcnt lgkmcnt(0)
	s_add_u32 s2, s10, s0
	v_and_b32_e32 v1, 3, v0
	s_addc_u32 s3, s11, s1
	s_mul_hi_u32 s1, s20, 0x18000
	s_mul_i32 s0, s20, 0x18000
	v_lshlrev_b32_e32 v104, 4, v0
	v_mov_b32_e32 v105, 0
	v_lshl_or_b32 v98, s18, 2, v1
	s_lshl_b64 s[18:19], s[0:1], 4
	v_lshl_add_u64 v[2:3], s[2:3], 0, v[104:105]
	s_add_u32 s0, s8, s18
	s_movk_i32 s8, 0x1000
	v_add_co_u32_e32 v10, vcc, s8, v2
	s_addc_u32 s1, s9, s19
	s_nop 0
	v_addc_co_u32_e32 v11, vcc, 0, v3, vcc
	global_load_dwordx4 v[2:5], v104, s[2:3]
	global_load_dwordx4 v[6:9], v[10:11], off
	s_mul_i32 s2, s20, 0x6000
	s_mul_hi_u32 s3, s20, 0x6000
	s_add_u32 s2, s12, s2
	s_addc_u32 s3, s13, s3
	v_lshl_add_u64 v[10:11], s[2:3], 0, v[104:105]
	s_movk_i32 s8, 0x2000
	v_add_co_u32_e32 v12, vcc, s8, v10
	s_movk_i32 s8, 0x3000
	s_nop 0
	v_addc_co_u32_e32 v13, vcc, 0, v11, vcc
	global_load_dwordx4 v[38:41], v104, s[2:3]
	global_load_dwordx4 v[42:45], v[12:13], off offset:-4096
	global_load_dwordx4 v[46:49], v[12:13], off
	v_add_co_u32_e32 v12, vcc, s8, v10
	v_lshrrev_b32_e32 v110, 2, v0
	s_nop 0
	v_addc_co_u32_e32 v13, vcc, 0, v11, vcc
	v_or_b32_e32 v14, 0x4000, v104
	global_load_dwordx4 v[50:53], v[12:13], off
	global_load_dwordx4 v[54:57], v14, s[2:3]
	s_movk_i32 s2, 0x5000
	v_add_co_u32_e32 v10, vcc, s2, v10
	s_movk_i32 s2, 0xc0
	v_or_b32_e32 v18, 64, v110
	v_addc_co_u32_e32 v11, vcc, 0, v11, vcc
	v_mov_b32_e32 v99, v105
	v_mad_u32_u24 v106, v110, s2, v98
	v_mov_b32_e32 v107, v105
	v_mul_u32_u24_e32 v102, 0xc00, v18
	v_mov_b32_e32 v103, v105
	global_load_dwordx4 v[66:69], v[10:11], off
	v_lshlrev_b64 v[10:11], 4, v[106:107]
	v_lshl_add_u64 v[14:15], s[0:1], 0, v[102:103]
	v_lshlrev_b64 v[16:17], 4, v[98:99]
	v_lshl_add_u64 v[12:13], s[0:1], 0, v[10:11]
	v_lshl_add_u64 v[14:15], v[14:15], 0, v[16:17]
	s_mov_b32 s3, 0x30000
	global_load_dwordx4 v[58:61], v[12:13], off
	global_load_dwordx4 v[62:65], v[14:15], off
	v_add_co_u32_e32 v12, vcc, s3, v14
	s_mov_b32 s3, 0x60000
	s_nop 0
	v_addc_co_u32_e32 v13, vcc, 0, v15, vcc
	v_add_co_u32_e32 v14, vcc, s3, v14
	s_movk_i32 s2, 0xc00
	s_nop 0
	v_addc_co_u32_e32 v15, vcc, 0, v15, vcc
	global_load_dwordx4 v[70:73], v[12:13], off
	global_load_dwordx4 v[74:77], v[14:15], off
	v_mov_b32_e32 v12, 0x90000
	v_mad_u32_u24 v12, v18, s2, v12
	v_mov_b32_e32 v13, v105
	v_mov_b32_e32 v14, 0xc0000
	v_lshl_add_u64 v[12:13], s[0:1], 0, v[12:13]
	v_mad_u32_u24 v100, v18, s2, v14
	v_mov_b32_e32 v101, v105
	v_lshl_add_u64 v[12:13], v[12:13], 0, v[16:17]
	v_lshl_add_u64 v[14:15], s[0:1], 0, v[100:101]
	v_lshl_add_u64 v[14:15], v[14:15], 0, v[16:17]
	global_load_dwordx4 v[78:81], v[12:13], off
	global_load_dwordx4 v[82:85], v[14:15], off
	v_mov_b32_e32 v12, 0xf0000
	v_mad_u32_u24 v96, v18, s2, v12
	v_mov_b32_e32 v97, v105
	v_mov_b32_e32 v14, 0x120000
	v_lshl_add_u64 v[12:13], s[0:1], 0, v[96:97]
	v_mad_u32_u24 v94, v18, s2, v14
	v_mov_b32_e32 v95, v105
	v_lshl_add_u64 v[12:13], v[12:13], 0, v[16:17]
	v_lshl_add_u64 v[14:15], s[0:1], 0, v[94:95]
	v_lshl_add_u64 v[14:15], v[14:15], 0, v[16:17]
	global_load_dwordx4 v[86:89], v[12:13], off
	global_load_dwordx4 v[90:93], v[14:15], off
	s_waitcnt vmcnt(15)
	ds_write_b128 v104, v[2:5] offset:57408
	s_waitcnt vmcnt(14)
	ds_write_b128 v104, v[6:9] offset:61504
	v_lshl_add_u64 v[2:3], s[6:7], 0, v[10:11]
	s_waitcnt lgkmcnt(0)
	s_barrier
	global_load_dwordx4 v[34:37], v[2:3], off
	v_lshl_add_u64 v[2:3], s[4:5], 0, v[10:11]
	v_add_u32_e32 v4, 0x3000, v106
	v_mov_b32_e32 v5, v105
	v_lshl_add_u64 v[4:5], v[4:5], 4, s[4:5]
	global_load_dwordx4 v[30:33], v[2:3], off
	global_load_dwordx4 v[26:29], v[4:5], off
	v_add_u32_e32 v2, 0x6000, v106
	v_mov_b32_e32 v3, v105
	v_lshl_add_u64 v[2:3], v[2:3], 4, s[4:5]
	v_add_u32_e32 v4, 0x9000, v106
	v_mov_b32_e32 v5, v105
	v_lshl_add_u64 v[4:5], v[4:5], 4, s[4:5]
	global_load_dwordx4 v[22:25], v[2:3], off
	global_load_dwordx4 v[18:21], v[4:5], off
	v_add_u32_e32 v2, 0xc000, v106
	v_mov_b32_e32 v3, v105
	v_lshl_add_u64 v[2:3], v[2:3], 4, s[4:5]
	v_add_u32_e32 v4, 0xf000, v106
	v_mov_b32_e32 v5, v105
	v_lshl_add_u64 v[4:5], v[4:5], 4, s[4:5]
	global_load_dwordx4 v[14:17], v[2:3], off
	global_load_dwordx4 v[10:13], v[4:5], off
	v_add_u32_e32 v2, 0x12000, v106
	v_mov_b32_e32 v3, v105
	v_lshl_add_u64 v[108:109], v[2:3], 4, s[4:5]
	v_add_u32_e32 v2, 0x15000, v106
	v_lshl_add_u64 v[106:107], v[2:3], 4, s[4:5]
	global_load_dwordx4 v[6:9], v[108:109], off
	global_load_dwordx4 v[2:5], v[106:107], off
	v_bfe_u32 v113, v0, 5, 1
	v_lshrrev_b32_e32 v115, 6, v0
	v_lshlrev_b32_e32 v112, 2, v113
	v_and_b32_e32 v111, 31, v0
	v_or_b32_e32 v116, v112, v115
	v_lshl_or_b32 v120, v116, 5, v111
	v_lshlrev_b32_e32 v108, 4, v120
	ds_read_b32 v140, v108 offset:57420
	ds_read_b32 v141, v108 offset:61516
	v_lshlrev_b32_e32 v142, 9, v116
	v_add_u32_e32 v142, 0x200, v142
	v_add_u32_e32 v143, 0x1000, v142
	v_mov_b32_e32 v152, 0x2000
	s_waitcnt lgkmcnt(0)
	v_ffbl_b32_e32 v153, v140
	v_ffbl_b32_e32 v154, v141
	v_cmp_ne_u32_e32 vcc, 0, v140
	v_cmp_ne_u32_e64 s[22:23], 0, v141
	v_lshl_add_u32 v153, v153, 4, v142
	v_lshl_add_u32 v154, v154, 4, v143
	v_cndmask_b32_e32 v144, v152, v153, vcc
	v_cndmask_b32_e64 v148, v152, v154, s[22:23]
	v_add_u32_e32 v153, -1, v140
	v_add_u32_e32 v154, -1, v141
	v_and_b32_e32 v140, v153, v140
	v_and_b32_e32 v141, v154, v141
	v_ffbl_b32_e32 v153, v140
	v_ffbl_b32_e32 v154, v141
	v_cmp_ne_u32_e32 vcc, 0, v140
	v_cmp_ne_u32_e64 s[22:23], 0, v141
	v_lshl_add_u32 v153, v153, 4, v142
	v_lshl_add_u32 v154, v154, 4, v143
	v_cndmask_b32_e32 v145, v152, v153, vcc
	v_cndmask_b32_e64 v149, v152, v154, s[22:23]
	v_add_u32_e32 v153, -1, v140
	v_add_u32_e32 v154, -1, v141
	v_and_b32_e32 v140, v153, v140
	v_and_b32_e32 v141, v154, v141
	v_ffbl_b32_e32 v153, v140
	v_ffbl_b32_e32 v154, v141
	v_cmp_ne_u32_e32 vcc, 0, v140
	v_cmp_ne_u32_e64 s[22:23], 0, v141
	v_lshl_add_u32 v153, v153, 4, v142
	v_lshl_add_u32 v154, v154, 4, v143
	v_cndmask_b32_e32 v146, v152, v153, vcc
	v_cndmask_b32_e64 v150, v152, v154, s[22:23]
	v_add_u32_e32 v153, -1, v140
	v_add_u32_e32 v154, -1, v141
	v_and_b32_e32 v140, v153, v140
	v_and_b32_e32 v141, v154, v141
	v_ffbl_b32_e32 v153, v140
	v_ffbl_b32_e32 v154, v141
	v_cmp_ne_u32_e32 vcc, 0, v140
	v_cmp_ne_u32_e64 s[22:23], 0, v141
	v_lshl_add_u32 v153, v153, 4, v142
	v_lshl_add_u32 v154, v154, 4, v143
	v_cndmask_b32_e32 v147, v152, v153, vcc
	v_cndmask_b32_e64 v151, v152, v154, s[22:23]
	v_add_u32_e32 v153, -1, v140
	v_add_u32_e32 v154, -1, v141
	v_and_b32_e32 v140, v153, v140
	v_and_b32_e32 v141, v154, v141
	v_lshl_or_b32 v144, v145, 16, v144
	v_lshl_or_b32 v145, v147, 16, v146
	v_lshl_or_b32 v148, v149, 16, v148
	v_lshl_or_b32 v149, v151, 16, v150
	v_lshrrev_b32_e32 v153, 1, v108
	v_add_u32_e32 v153, 0x118c0, v153
	v_lshrrev_b32_e32 v154, 2, v108
	v_add_u32_e32 v154, 0x128c0, v154
	ds_write_b64 v153, v[144:145]
	ds_write_b64 v153, v[148:149] offset:2048
	ds_write_b32 v154, v140
	ds_write_b32 v154, v141 offset:1024
	ds_read_b64 v[106:107], v108 offset:57408
	ds_read_u16 v118, v108 offset:57410
	v_and_b32_e32 v114, 63, v0
	v_and_b32_e32 v0, 32, v0
	v_add_u32_e32 v117, 0xe040, v108
	v_mov_b32_e32 v108, -1
	v_mov_b32_e32 v119, v105
	s_branch .LBB2_2

.LBB2_12:
	s_or_b64 exec, exec, s[12:13]
	v_lshlrev_b32_e32 v106, 9, v119
	v_ffbl_b32_e32 v107, v107
	v_ffbl_b32_e32 v108, v108
	v_lshlrev_b32_e32 v116, 25, v119
	v_lshl_or_b32 v107, v107, 4, v106
	v_mov_b32_e32 v109, 0x2000
	v_lshl_or_b32 v108, v108, 20, v116
	v_bfrev_b32_e32 v116, 4
	v_ffbl_b32_e32 v0, v0
	v_cndmask_b32_e64 v107, v107, v109, s[8:9]
	v_cndmask_b32_e64 v108, v108, v116, s[4:5]
	v_lshl_or_b32 v0, v0, 4, v106
	v_cndmask_b32_e32 v0, v0, v109, vcc
	v_or_b32_e32 v106, v108, v107
	v_mov_b32_e32 v108, 0x800000
	v_lshlrev_b32_e32 v107, 16, v117
	v_cndmask_b32_e64 v108, 0, v108, s[6:7]
	s_waitcnt lgkmcnt(2)
	v_lshl_or_b32 v0, v118, 24, v0
	v_or3_b32 v0, v0, v108, v107
	ds_write2_b32 v105, v106, v0 offset0:1 offset1:3
	v_cmp_ne_u32_e32 vcc, 0, v140
	v_cmp_ne_u32_e64 s[22:23], 0, v141
	v_lshlrev_b32_e32 v150, 5, v113
	v_lshl_add_u32 v155, v113, 2, v115
	v_lshlrev_b32_e32 v155, 2, v155
	v_add_u32_e32 v155, 0x11840, v155
	v_lshrrev_b64 v[146:147], v150, vcc
	v_lshrrev_b64 v[156:157], v150, s[22:23]
	v_mov_b32_e32 v151, 0x400
	v_cmp_ne_u32_e32 vcc, 0, v146
	v_cmp_ne_u32_e64 s[22:23], 0, v156
	s_nop 1
	v_cndmask_b32_e32 v146, 0, v151, vcc
	v_cndmask_b32_e64 v156, 0, v151, s[22:23]
	v_cmp_eq_u32_e32 vcc, 0, v111
	s_and_saveexec_b64 s[22:23], vcc
	ds_or_b32 v155, v146
	ds_or_b32 v155, v156 offset:32
	s_or_b64 exec, exec, s[22:23]
	s_movk_i32 s2, 0x2010
	v_mul_u32_u24_e32 v105, 0x2010, v115
	v_cmp_eq_u32_e32 vcc, 0, v114
	s_waitcnt vmcnt(22)
	ds_write_b128 v104, v[38:41] offset:32832
	s_waitcnt vmcnt(21)
	ds_write_b128 v104, v[42:45] offset:36928
	s_waitcnt vmcnt(20)
	ds_write_b128 v104, v[46:49] offset:41024
	s_waitcnt vmcnt(19)
	ds_write_b128 v104, v[50:53] offset:45120
	s_waitcnt vmcnt(18)
	ds_write_b128 v104, v[54:57] offset:49216
	s_waitcnt vmcnt(17)
	ds_write_b128 v104, v[66:69] offset:53312
	s_and_saveexec_b64 s[0:1], vcc
	v_mov_b32_e32 v38, 0
	v_mov_b32_e32 v39, v38
	v_mov_b32_e32 v40, v38
	v_mov_b32_e32 v41, v38
	ds_write_b128 v105, v[38:41] offset:8192
	s_or_b64 exec, exec, s[0:1]
	v_lshlrev_b32_e32 v40, 3, v113
	v_lshlrev_b32_e32 v67, 4, v110
	v_or_b32_e32 v38, 0x1e0, v111
	v_or_b32_e32 v0, 0x8040, v40
	v_mad_u32_u24 v66, v1, s2, v67
	v_mad_u32_u24 v38, v38, 48, v0
	s_waitcnt vmcnt(16)
	ds_write_b128 v66, v[58:61]
	s_waitcnt vmcnt(15)
	ds_write_b128 v66, v[62:65] offset:1024
	s_waitcnt vmcnt(14)
	ds_write_b128 v66, v[70:73] offset:2048
	s_waitcnt vmcnt(13)
	ds_write_b128 v66, v[74:77] offset:3072
	s_waitcnt vmcnt(12)
	ds_write_b128 v66, v[78:81] offset:4096
	s_waitcnt vmcnt(11)
	ds_write_b128 v66, v[82:85] offset:5120
	s_waitcnt vmcnt(10)
	ds_write_b128 v66, v[86:89] offset:6144
	s_waitcnt vmcnt(9)
	ds_write_b128 v66, v[90:93] offset:7168
	s_waitcnt lgkmcnt(0)
	s_barrier
	v_lshl_add_u32 v116, v113, 3, v105
	v_or_b32_e32 v106, 0x1e0, v111
	v_lshlrev_b32_e32 v138, 4, v106
	v_lshlrev_b32_e32 v139, 3, v106
	v_add_u32_e32 v139, 0x118c0, v139
	v_mul_u32_u24_e32 v156, 48, v106
	v_add_u32_e32 v156, v0, v156
	v_mov_b32_e32 v157, 0x1187c
	v_add_u32_e32 v137, v116, v138
	v_add_u32_e32 v138, 0x200, v138
	v_lshlrev_b32_e32 v160, 4, v111
	v_lshlrev_b32_e32 v161, 3, v111
	v_add_u32_e32 v161, 0x118c0, v161
	v_mul_u32_u24_e32 v162, 48, v111
	v_add_u32_e32 v162, v0, v162
	v_mov_b32_e32 v163, 0x11840
	v_mul_hi_u32_u24_e32 v159, 0x410, v111
	v_mul_u32_u24_e32 v158, 0x410, v111
	v_mov_b32_e32 v107, 0x82000
	v_mad_u64_u32 v[158:159], s[0:1], s20, v107, v[158:159]
	v_lshlrev_b32_e32 v107, 3, v113
	v_or_b32_e32 v158, v158, v107
	v_lshl_add_u64 v[158:159], s[14:15], 0, v[158:159]
	s_mov_b64 s[0:1], 0x79e30
	s_mov_b32 s2, 0xffff7e00
	s_mov_b32 s3, -1
	v_lshl_add_u64 v[158:159], v[158:159], 0, s[0:1]
	ds_read_b128 v[38:41], v138 offset:56896
	ds_read_b64 v[42:43], v139
	ds_read2_b64 v[56:59], v156 offset1:2
	ds_read_b32 v60, v157
	v_add_u32_e32 v156, 0xfffffa00, v156
	v_add_u32_e32 v157, -4, v157
	ds_read2_b64 v[52:55], v156 offset1:2
	ds_read_b32 v64, v157
	s_waitcnt lgkmcnt(0)
	v_readfirstlane_b32 s4, v60
	v_readfirstlane_b32 s21, v64
	v_add_u32_sdwa v92, v105, v56 dst_sel:DWORD dst_unused:UNUSED_PAD src0_sel:DWORD src1_sel:WORD_0
	v_add_u32_sdwa v93, v105, v56 dst_sel:DWORD dst_unused:UNUSED_PAD src0_sel:DWORD src1_sel:WORD_1
	v_add_u32_sdwa v106, v105, v57 dst_sel:DWORD dst_unused:UNUSED_PAD src0_sel:DWORD src1_sel:WORD_0
	v_add_u32_sdwa v107, v105, v57 dst_sel:DWORD dst_unused:UNUSED_PAD src0_sel:DWORD src1_sel:WORD_1
	v_add_u32_sdwa v108, v105, v58 dst_sel:DWORD dst_unused:UNUSED_PAD src0_sel:DWORD src1_sel:WORD_0
	v_add_u32_sdwa v109, v105, v58 dst_sel:DWORD dst_unused:UNUSED_PAD src0_sel:DWORD src1_sel:WORD_1
	v_add_u32_sdwa v88, v105, v59 dst_sel:DWORD dst_unused:UNUSED_PAD src0_sel:DWORD src1_sel:WORD_0
	v_add_u32_sdwa v89, v105, v59 dst_sel:DWORD dst_unused:UNUSED_PAD src0_sel:DWORD src1_sel:WORD_1
	ds_read_b128 v[120:123], v92
	ds_read_b128 v[124:127], v93
	ds_read_b128 v[128:131], v106
	ds_read_b128 v[132:135], v107
	ds_read_b128 v[140:143], v108
	ds_read_b128 v[144:147], v109
	ds_read_b128 v[148:151], v88
	ds_read_b128 v[152:155], v89
	s_waitcnt lgkmcnt(0)
	v_pk_add_f32 v[120:121], v[120:121], v[124:125]
	v_pk_add_f32 v[122:123], v[122:123], v[126:127]
	v_pk_add_f32 v[128:129], v[128:129], v[132:133]
	v_pk_add_f32 v[130:131], v[130:131], v[134:135]
	v_pk_add_f32 v[140:141], v[140:141], v[144:145]
	v_pk_add_f32 v[142:143], v[142:143], v[146:147]
	v_pk_add_f32 v[148:149], v[148:149], v[152:153]
	v_pk_add_f32 v[150:151], v[150:151], v[154:155]
	s_bitcmp1_b32 s4, 8
	s_cbranch_scc1 .Lfarslow_pre

.Lchain_top:
	s_or_b32 s10, s4, s21
	s_and_b32 s10, s10, 0x700
	s_cbranch_scc1 .Lit_As
	s_and_b32 s9, s4, 0xff
	s_cbranch_scc0 .Lit_As
.Lit_Af:
	v_add_u32_sdwa v88, v116, v42 dst_sel:DWORD dst_unused:UNUSED_PAD src0_sel:DWORD src1_sel:WORD_0
	v_add_u32_sdwa v89, v116, v42 dst_sel:DWORD dst_unused:UNUSED_PAD src0_sel:DWORD src1_sel:WORD_1
	ds_read_b64 v[68:69], v88
	v_add_u32_sdwa v90, v116, v43 dst_sel:DWORD dst_unused:UNUSED_PAD src0_sel:DWORD src1_sel:WORD_0
	ds_read_b64 v[70:71], v89
	v_add_u32_sdwa v91, v116, v43 dst_sel:DWORD dst_unused:UNUSED_PAD src0_sel:DWORD src1_sel:WORD_1
	ds_read_b64 v[72:73], v90
	ds_read_b64 v[74:75], v91
	v_add_u32_sdwa v92, v105, v52 dst_sel:DWORD dst_unused:UNUSED_PAD src0_sel:DWORD src1_sel:WORD_0
	v_add_u32_sdwa v93, v105, v52 dst_sel:DWORD dst_unused:UNUSED_PAD src0_sel:DWORD src1_sel:WORD_1
	v_add_u32_sdwa v106, v105, v53 dst_sel:DWORD dst_unused:UNUSED_PAD src0_sel:DWORD src1_sel:WORD_0
	v_add_u32_sdwa v107, v105, v53 dst_sel:DWORD dst_unused:UNUSED_PAD src0_sel:DWORD src1_sel:WORD_1
	v_add_u32_sdwa v108, v105, v54 dst_sel:DWORD dst_unused:UNUSED_PAD src0_sel:DWORD src1_sel:WORD_0
	v_add_u32_sdwa v109, v105, v54 dst_sel:DWORD dst_unused:UNUSED_PAD src0_sel:DWORD src1_sel:WORD_1
	v_add_u32_sdwa v88, v105, v55 dst_sel:DWORD dst_unused:UNUSED_PAD src0_sel:DWORD src1_sel:WORD_0
	v_add_u32_sdwa v89, v105, v55 dst_sel:DWORD dst_unused:UNUSED_PAD src0_sel:DWORD src1_sel:WORD_1
	ds_read_b128 v[120:123], v92
	ds_read_b128 v[124:127], v93
	ds_read_b128 v[128:131], v106
	ds_read_b128 v[132:135], v107
	ds_read_b128 v[140:143], v108
	ds_read_b128 v[144:147], v109
	ds_read_b128 v[148:151], v88
	ds_read_b128 v[152:155], v89
	v_add_u32_sdwa v118, v116, v39 dst_sel:DWORD dst_unused:UNUSED_PAD src0_sel:DWORD src1_sel:WORD_0
	s_waitcnt lgkmcnt(11)
	v_pk_add_f32 v[76:77], v[44:45], v[68:69]
	s_waitcnt lgkmcnt(9)
	v_pk_add_f32 v[78:79], v[70:71], v[72:73]
	s_waitcnt lgkmcnt(8)
	v_pk_add_f32 v[76:77], v[76:77], v[74:75]
	v_bfe_u32 v117, v41, 16, 7
	v_pk_add_f32 v[76:77], v[76:77], v[78:79]
	v_add_u32_sdwa v119, v116, v39 dst_sel:DWORD dst_unused:UNUSED_PAD src0_sel:DWORD src1_sel:WORD_1
	v_pk_mul_f32 v[78:79], v[40:41], v[76:77] op_sel_hi:[0,1]
	v_cmp_eq_u32_e32 vcc, 0, v117
	v_add_u32_sdwa v136, v116, v41 dst_sel:DWORD dst_unused:UNUSED_PAD src0_sel:DWORD src1_sel:WORD_0
	s_mov_b64 exec, vcc
	ds_write_b64 v137, v[78:79]
	s_mov_b64 exec, -1
	ds_read_b128 v[46:49], v138 offset:56896
	ds_read_b64 v[50:51], v139
	ds_read2_b64 v[56:59], v156 offset1:2
	ds_read_b32 v60, v157
	v_cmp_eq_u32_e64 s[6:7], 1, v117
	s_waitcnt lgkmcnt(4)
	s_mov_b64 exec, s[6:7]
	ds_read_b64 v[82:83], v118
	ds_read_b64 v[84:85], v119
	ds_read_b64 v[86:87], v136
	s_mov_b64 exec, -1
	v_pk_add_f32 v[120:121], v[120:121], v[124:125]
	v_pk_add_f32 v[122:123], v[122:123], v[126:127]
	v_pk_add_f32 v[128:129], v[128:129], v[132:133]
	v_pk_add_f32 v[130:131], v[130:131], v[134:135]
	v_pk_add_f32 v[140:141], v[140:141], v[144:145]
	v_pk_add_f32 v[142:143], v[142:143], v[146:147]
	v_pk_add_f32 v[148:149], v[148:149], v[152:153]
	v_pk_add_f32 v[150:151], v[150:151], v[154:155]
	v_pk_add_f32 v[120:121], v[120:121], v[128:129]
	v_pk_add_f32 v[122:123], v[122:123], v[130:131]
	v_pk_add_f32 v[140:141], v[140:141], v[148:149]
	v_pk_add_f32 v[142:143], v[142:143], v[150:151]
	v_pk_add_f32 v[120:121], v[120:121], v[140:141]
	v_pk_add_f32 v[122:123], v[122:123], v[142:143]
	s_nop 1
	v_permlane32_swap_b32_e32 v120, v122
	v_permlane32_swap_b32_e32 v121, v123
	v_pk_add_f32 v[62:63], v[120:121], v[122:123]
	s_mov_b64 exec, s[6:7]
	s_waitcnt lgkmcnt(2)
	v_pk_fma_f32 v[80:81], v[40:41], v[82:83], v[78:79] op_sel_hi:[0,1,1]
	s_waitcnt lgkmcnt(1)
	v_pk_fma_f32 v[80:81], v[40:41], v[84:85], v[80:81] op_sel_hi:[0,1,1]
	s_waitcnt lgkmcnt(0)
	v_pk_fma_f32 v[80:81], v[40:41], v[86:87], v[80:81] op_sel_hi:[0,1,1]
	ds_write_b64 v137, v[80:81]
	s_mov_b64 exec, -1
	s_cmp_lt_u32 s9, 2
	s_cbranch_scc1 .Lend_A
	s_mov_b32 s8, 2

.Lend_A:
	s_waitcnt lgkmcnt(0)
	v_add_u32_e32 v138, 0xfffffe00, v138
	v_add_u32_e32 v139, 0xffffff00, v139
	v_add_u32_e32 v156, 0xfffffa00, v156
	v_add_u32_e32 v157, -4, v157
	v_add_u32_e32 v137, 0xfffffe00, v137
	v_max_i32_e32 v156, v156, v162
	v_lshl_add_u64 v[158:159], v[158:159], 0, s[2:3]
	v_readfirstlane_b32 s4, v60
	s_sub_u32 s5, s5, 1
	s_or_b32 s10, s21, s4
	s_and_b32 s10, s10, 0x700
	s_cbranch_scc1 .Lit_Bs
	s_and_b32 s9, s21, 0xff
	s_cbranch_scc0 .Lit_Bs
.Lit_Bf:
	v_add_u32_sdwa v88, v116, v50 dst_sel:DWORD dst_unused:UNUSED_PAD src0_sel:DWORD src1_sel:WORD_0
	v_add_u32_sdwa v89, v116, v50 dst_sel:DWORD dst_unused:UNUSED_PAD src0_sel:DWORD src1_sel:WORD_1
	ds_read_b64 v[68:69], v88
	v_add_u32_sdwa v90, v116, v51 dst_sel:DWORD dst_unused:UNUSED_PAD src0_sel:DWORD src1_sel:WORD_0
	ds_read_b64 v[70:71], v89
	v_add_u32_sdwa v91, v116, v51 dst_sel:DWORD dst_unused:UNUSED_PAD src0_sel:DWORD src1_sel:WORD_1
	ds_read_b64 v[72:73], v90
	ds_read_b64 v[74:75], v91
	v_add_u32_sdwa v92, v105, v56 dst_sel:DWORD dst_unused:UNUSED_PAD src0_sel:DWORD src1_sel:WORD_0
	v_add_u32_sdwa v93, v105, v56 dst_sel:DWORD dst_unused:UNUSED_PAD src0_sel:DWORD src1_sel:WORD_1
	v_add_u32_sdwa v106, v105, v57 dst_sel:DWORD dst_unused:UNUSED_PAD src0_sel:DWORD src1_sel:WORD_0
	v_add_u32_sdwa v107, v105, v57 dst_sel:DWORD dst_unused:UNUSED_PAD src0_sel:DWORD src1_sel:WORD_1
	v_add_u32_sdwa v108, v105, v58 dst_sel:DWORD dst_unused:UNUSED_PAD src0_sel:DWORD src1_sel:WORD_0
	v_add_u32_sdwa v109, v105, v58 dst_sel:DWORD dst_unused:UNUSED_PAD src0_sel:DWORD src1_sel:WORD_1
	v_add_u32_sdwa v88, v105, v59 dst_sel:DWORD dst_unused:UNUSED_PAD src0_sel:DWORD src1_sel:WORD_0
	v_add_u32_sdwa v89, v105, v59 dst_sel:DWORD dst_unused:UNUSED_PAD src0_sel:DWORD src1_sel:WORD_1
	ds_read_b128 v[120:123], v92
	ds_read_b128 v[124:127], v93
	ds_read_b128 v[128:131], v106
	ds_read_b128 v[132:135], v107
	ds_read_b128 v[140:143], v108
	ds_read_b128 v[144:147], v109
	ds_read_b128 v[148:151], v88
	ds_read_b128 v[152:155], v89
	v_add_u32_sdwa v118, v116, v47 dst_sel:DWORD dst_unused:UNUSED_PAD src0_sel:DWORD src1_sel:WORD_0
	s_waitcnt lgkmcnt(11)
	v_pk_add_f32 v[76:77], v[62:63], v[68:69]
	s_waitcnt lgkmcnt(9)
	v_pk_add_f32 v[78:79], v[70:71], v[72:73]
	s_waitcnt lgkmcnt(8)
	v_pk_add_f32 v[76:77], v[76:77], v[74:75]
	v_bfe_u32 v117, v49, 16, 7
	v_pk_add_f32 v[76:77], v[76:77], v[78:79]
	v_add_u32_sdwa v119, v116, v47 dst_sel:DWORD dst_unused:UNUSED_PAD src0_sel:DWORD src1_sel:WORD_1
	v_pk_mul_f32 v[78:79], v[48:49], v[76:77] op_sel_hi:[0,1]
	v_cmp_eq_u32_e32 vcc, 0, v117
	v_add_u32_sdwa v136, v116, v49 dst_sel:DWORD dst_unused:UNUSED_PAD src0_sel:DWORD src1_sel:WORD_0
	s_mov_b64 exec, vcc
	ds_write_b64 v137, v[78:79]
	s_mov_b64 exec, -1
	ds_read_b128 v[38:41], v138 offset:56896
	ds_read_b64 v[42:43], v139
	ds_read2_b64 v[52:55], v156 offset1:2
	ds_read_b32 v60, v157
	v_cmp_eq_u32_e64 s[6:7], 1, v117
	s_waitcnt lgkmcnt(4)
	s_mov_b64 exec, s[6:7]
	ds_read_b64 v[82:83], v118
	ds_read_b64 v[84:85], v119
	ds_read_b64 v[86:87], v136
	s_mov_b64 exec, -1
	v_pk_add_f32 v[120:121], v[120:121], v[124:125]
	v_pk_add_f32 v[122:123], v[122:123], v[126:127]
	v_pk_add_f32 v[128:129], v[128:129], v[132:133]
	v_pk_add_f32 v[130:131], v[130:131], v[134:135]
	v_pk_add_f32 v[140:141], v[140:141], v[144:145]
	v_pk_add_f32 v[142:143], v[142:143], v[146:147]
	v_pk_add_f32 v[148:149], v[148:149], v[152:153]
	v_pk_add_f32 v[150:151], v[150:151], v[154:155]
	v_pk_add_f32 v[120:121], v[120:121], v[128:129]
	v_pk_add_f32 v[122:123], v[122:123], v[130:131]
	v_pk_add_f32 v[140:141], v[140:141], v[148:149]
	v_pk_add_f32 v[142:143], v[142:143], v[150:151]
	v_pk_add_f32 v[120:121], v[120:121], v[140:141]
	v_pk_add_f32 v[122:123], v[122:123], v[142:143]
	s_nop 1
	v_permlane32_swap_b32_e32 v120, v122
	v_permlane32_swap_b32_e32 v121, v123
	v_pk_add_f32 v[44:45], v[120:121], v[122:123]
	s_mov_b64 exec, s[6:7]
	s_waitcnt lgkmcnt(2)
	v_pk_fma_f32 v[80:81], v[48:49], v[82:83], v[78:79] op_sel_hi:[0,1,1]
	s_waitcnt lgkmcnt(1)
	v_pk_fma_f32 v[80:81], v[48:49], v[84:85], v[80:81] op_sel_hi:[0,1,1]
	s_waitcnt lgkmcnt(0)
	v_pk_fma_f32 v[80:81], v[48:49], v[86:87], v[80:81] op_sel_hi:[0,1,1]
	ds_write_b64 v137, v[80:81]
	s_mov_b64 exec, -1
	s_cmp_lt_u32 s9, 2
	s_cbranch_scc1 .Lend_B
	s_mov_b32 s8, 2

.Lend_B:
	s_waitcnt lgkmcnt(0)
	v_add_u32_e32 v138, 0xfffffe00, v138
	v_add_u32_e32 v139, 0xffffff00, v139
	v_add_u32_e32 v156, 0xfffffa00, v156
	v_add_u32_e32 v157, -4, v157
	v_add_u32_e32 v137, 0xfffffe00, v137
	v_max_i32_e32 v156, v156, v162
	v_lshl_add_u64 v[158:159], v[158:159], 0, s[2:3]
	v_readfirstlane_b32 s21, v60
	s_cmp_eq_u32 s5, 0
	s_cbranch_scc1 .Lchain_done
	s_sub_u32 s5, s5, 1
	s_branch .Lchain_top
.Lit_As:
	v_add_u32_sdwa v88, v116, v42 dst_sel:DWORD dst_unused:UNUSED_PAD src0_sel:DWORD src1_sel:WORD_0
	v_add_u32_sdwa v89, v116, v42 dst_sel:DWORD dst_unused:UNUSED_PAD src0_sel:DWORD src1_sel:WORD_1
	ds_read_b64 v[68:69], v88
	v_add_u32_sdwa v90, v116, v43 dst_sel:DWORD dst_unused:UNUSED_PAD src0_sel:DWORD src1_sel:WORD_0
	ds_read_b64 v[70:71], v89
	v_add_u32_sdwa v91, v116, v43 dst_sel:DWORD dst_unused:UNUSED_PAD src0_sel:DWORD src1_sel:WORD_1
	ds_read_b64 v[72:73], v90
	ds_read_b64 v[74:75], v91
	v_add_u32_sdwa v92, v105, v52 dst_sel:DWORD dst_unused:UNUSED_PAD src0_sel:DWORD src1_sel:WORD_0
	v_add_u32_sdwa v93, v105, v52 dst_sel:DWORD dst_unused:UNUSED_PAD src0_sel:DWORD src1_sel:WORD_1
	v_add_u32_sdwa v106, v105, v53 dst_sel:DWORD dst_unused:UNUSED_PAD src0_sel:DWORD src1_sel:WORD_0
	v_add_u32_sdwa v107, v105, v53 dst_sel:DWORD dst_unused:UNUSED_PAD src0_sel:DWORD src1_sel:WORD_1
	v_add_u32_sdwa v108, v105, v54 dst_sel:DWORD dst_unused:UNUSED_PAD src0_sel:DWORD src1_sel:WORD_0
	v_add_u32_sdwa v109, v105, v54 dst_sel:DWORD dst_unused:UNUSED_PAD src0_sel:DWORD src1_sel:WORD_1
	v_add_u32_sdwa v88, v105, v55 dst_sel:DWORD dst_unused:UNUSED_PAD src0_sel:DWORD src1_sel:WORD_0
	v_add_u32_sdwa v89, v105, v55 dst_sel:DWORD dst_unused:UNUSED_PAD src0_sel:DWORD src1_sel:WORD_1
	ds_read_b128 v[120:123], v92
	ds_read_b128 v[124:127], v93
	ds_read_b128 v[128:131], v106
	ds_read_b128 v[132:135], v107
	ds_read_b128 v[140:143], v108
	ds_read_b128 v[144:147], v109
	ds_read_b128 v[148:151], v88
	ds_read_b128 v[152:155], v89
	v_add_u32_sdwa v118, v116, v39 dst_sel:DWORD dst_unused:UNUSED_PAD src0_sel:DWORD src1_sel:WORD_0
	s_waitcnt lgkmcnt(11)
	v_pk_add_f32 v[76:77], v[44:45], v[68:69]
	s_waitcnt lgkmcnt(9)
	v_pk_add_f32 v[78:79], v[70:71], v[72:73]
	s_waitcnt lgkmcnt(8)
	v_pk_add_f32 v[76:77], v[76:77], v[74:75]
	v_bfe_u32 v117, v41, 16, 7
	v_pk_add_f32 v[76:77], v[76:77], v[78:79]
	v_add_u32_sdwa v119, v116, v39 dst_sel:DWORD dst_unused:UNUSED_PAD src0_sel:DWORD src1_sel:WORD_1
	s_bitcmp1_b32 s4, 10
	s_cbranch_scc1 .Lnearslow_As
.Lnearslow_ret_As:
	v_pk_mul_f32 v[78:79], v[40:41], v[76:77] op_sel_hi:[0,1]
	v_cmp_eq_u32_e32 vcc, 0, v117
	v_add_u32_sdwa v136, v116, v41 dst_sel:DWORD dst_unused:UNUSED_PAD src0_sel:DWORD src1_sel:WORD_0
	s_mov_b64 exec, vcc
	ds_write_b64 v137, v[78:79]
	s_mov_b64 exec, -1
	ds_read_b128 v[46:49], v138 offset:56896
	ds_read_b64 v[50:51], v139
	ds_read2_b64 v[56:59], v156 offset1:2
	ds_read_b32 v60, v157
	s_and_b32 s9, s4, 0xff
	v_cmp_eq_u32_e64 s[6:7], 1, v117
	s_waitcnt lgkmcnt(4)
	s_bitcmp1_b32 s4, 9
	s_cbranch_scc1 .Lfs_As
	s_cmp_eq_u32 s9, 0
	s_cbranch_scc1 .Lfs_As
	s_mov_b64 exec, s[6:7]
	ds_read_b64 v[82:83], v118
	ds_read_b64 v[84:85], v119
	ds_read_b64 v[86:87], v136
	s_mov_b64 exec, -1

.Llev_As:
	v_cmp_eq_u32_e64 s[6:7], s8, v117
	s_add_u32 s8, s8, 1
	s_mov_b64 exec, s[6:7]
	ds_read_b64 v[82:83], v118
	ds_read_b64 v[84:85], v119
	ds_read_b64 v[86:87], v136
	s_waitcnt lgkmcnt(2)
	v_pk_fma_f32 v[80:81], v[40:41], v[82:83], v[78:79] op_sel_hi:[0,1,1]
	s_waitcnt lgkmcnt(1)
	v_pk_fma_f32 v[80:81], v[40:41], v[84:85], v[80:81] op_sel_hi:[0,1,1]
	s_waitcnt lgkmcnt(0)
	v_pk_fma_f32 v[80:81], v[40:41], v[86:87], v[80:81] op_sel_hi:[0,1,1]
	ds_write_b64 v137, v[80:81]
	s_mov_b64 exec, -1
	s_cmp_le_u32 s8, s9
	s_cbranch_scc1 .Llev_As
	s_branch .Lend_A
.Lit_Bs:
	v_add_u32_sdwa v88, v116, v50 dst_sel:DWORD dst_unused:UNUSED_PAD src0_sel:DWORD src1_sel:WORD_0
	v_add_u32_sdwa v89, v116, v50 dst_sel:DWORD dst_unused:UNUSED_PAD src0_sel:DWORD src1_sel:WORD_1
	ds_read_b64 v[68:69], v88
	v_add_u32_sdwa v90, v116, v51 dst_sel:DWORD dst_unused:UNUSED_PAD src0_sel:DWORD src1_sel:WORD_0
	ds_read_b64 v[70:71], v89
	v_add_u32_sdwa v91, v116, v51 dst_sel:DWORD dst_unused:UNUSED_PAD src0_sel:DWORD src1_sel:WORD_1
	ds_read_b64 v[72:73], v90
	ds_read_b64 v[74:75], v91
	v_add_u32_sdwa v92, v105, v56 dst_sel:DWORD dst_unused:UNUSED_PAD src0_sel:DWORD src1_sel:WORD_0
	v_add_u32_sdwa v93, v105, v56 dst_sel:DWORD dst_unused:UNUSED_PAD src0_sel:DWORD src1_sel:WORD_1
	v_add_u32_sdwa v106, v105, v57 dst_sel:DWORD dst_unused:UNUSED_PAD src0_sel:DWORD src1_sel:WORD_0
	v_add_u32_sdwa v107, v105, v57 dst_sel:DWORD dst_unused:UNUSED_PAD src0_sel:DWORD src1_sel:WORD_1
	v_add_u32_sdwa v108, v105, v58 dst_sel:DWORD dst_unused:UNUSED_PAD src0_sel:DWORD src1_sel:WORD_0
	v_add_u32_sdwa v109, v105, v58 dst_sel:DWORD dst_unused:UNUSED_PAD src0_sel:DWORD src1_sel:WORD_1
	v_add_u32_sdwa v88, v105, v59 dst_sel:DWORD dst_unused:UNUSED_PAD src0_sel:DWORD src1_sel:WORD_0
	v_add_u32_sdwa v89, v105, v59 dst_sel:DWORD dst_unused:UNUSED_PAD src0_sel:DWORD src1_sel:WORD_1
	ds_read_b128 v[120:123], v92
	ds_read_b128 v[124:127], v93
	ds_read_b128 v[128:131], v106
	ds_read_b128 v[132:135], v107
	ds_read_b128 v[140:143], v108
	ds_read_b128 v[144:147], v109
	ds_read_b128 v[148:151], v88
	ds_read_b128 v[152:155], v89
	v_add_u32_sdwa v118, v116, v47 dst_sel:DWORD dst_unused:UNUSED_PAD src0_sel:DWORD src1_sel:WORD_0
	s_waitcnt lgkmcnt(11)
	v_pk_add_f32 v[76:77], v[62:63], v[68:69]
	s_waitcnt lgkmcnt(9)
	v_pk_add_f32 v[78:79], v[70:71], v[72:73]
	s_waitcnt lgkmcnt(8)
	v_pk_add_f32 v[76:77], v[76:77], v[74:75]
	v_bfe_u32 v117, v49, 16, 7
	v_pk_add_f32 v[76:77], v[76:77], v[78:79]
	v_add_u32_sdwa v119, v116, v47 dst_sel:DWORD dst_unused:UNUSED_PAD src0_sel:DWORD src1_sel:WORD_1
	s_bitcmp1_b32 s21, 10
	s_cbranch_scc1 .Lnearslow_Bs
.Lnearslow_ret_Bs:
	v_pk_mul_f32 v[78:79], v[48:49], v[76:77] op_sel_hi:[0,1]
	v_cmp_eq_u32_e32 vcc, 0, v117
	v_add_u32_sdwa v136, v116, v49 dst_sel:DWORD dst_unused:UNUSED_PAD src0_sel:DWORD src1_sel:WORD_0
	s_mov_b64 exec, vcc
	ds_write_b64 v137, v[78:79]
	s_mov_b64 exec, -1
	ds_read_b128 v[38:41], v138 offset:56896
	ds_read_b64 v[42:43], v139
	ds_read2_b64 v[52:55], v156 offset1:2
	ds_read_b32 v60, v157
	s_and_b32 s9, s21, 0xff
	v_cmp_eq_u32_e64 s[6:7], 1, v117
	s_waitcnt lgkmcnt(4)
	s_bitcmp1_b32 s21, 9
	s_cbranch_scc1 .Lfs_Bs
	s_cmp_eq_u32 s9, 0
	s_cbranch_scc1 .Lfs_Bs
	s_mov_b64 exec, s[6:7]
	ds_read_b64 v[82:83], v118
	ds_read_b64 v[84:85], v119
	ds_read_b64 v[86:87], v136
	s_mov_b64 exec, -1

.Llev_Bs:
	v_cmp_eq_u32_e64 s[6:7], s8, v117
	s_add_u32 s8, s8, 1
	s_mov_b64 exec, s[6:7]
	ds_read_b64 v[82:83], v118
	ds_read_b64 v[84:85], v119
	ds_read_b64 v[86:87], v136
	s_waitcnt lgkmcnt(2)
	v_pk_fma_f32 v[80:81], v[48:49], v[82:83], v[78:79] op_sel_hi:[0,1,1]
	s_waitcnt lgkmcnt(1)
	v_pk_fma_f32 v[80:81], v[48:49], v[84:85], v[80:81] op_sel_hi:[0,1,1]
	s_waitcnt lgkmcnt(0)
	v_pk_fma_f32 v[80:81], v[48:49], v[86:87], v[80:81] op_sel_hi:[0,1,1]
	ds_write_b64 v137, v[80:81]
	s_mov_b64 exec, -1
	s_cmp_le_u32 s8, s9
	s_cbranch_scc1 .Llev_Bs
	s_branch .Lend_B
